# prologue de-serialisation: removed the dead LDS bias-table block (6 loads + 4 vmcnt waits + 2 LDS writes) from the MP0 and FIRST prologues so index loads issue without draining the weight loads
# speedup vs baseline: 1.0033x; 1.0033x over previous
.LBB5_4:
	s_or_b64 exec, exec, s[4:5]
	v_cmp_gt_u32_e32 vcc, 64, v0
	s_and_saveexec_b64 s[4:5], vcc
	s_cbranch_execz .LBB5_2

_Z10mp2_kernelILb0ELi1EEvPKDF16_PDF16_PKiPKfPKDv8_DF16_S6_S6_ii:
	v_lshrrev_b32_e32 v152, 6, v0
	s_load_dwordx4 s[8:11], s[0:1], 0x20
	s_load_dwordx2 s[4:5], s[0:1], 0x30
	v_readfirstlane_b32 s3, v152
	s_mul_i32 s6, s3, 29
	s_ashr_i32 s7, s6, 31
	s_lshl_b64 s[6:7], s[6:7], 10
	v_and_b32_e32 v1, 63, v0
	s_waitcnt lgkmcnt(0)
	s_add_u32 s6, s8, s6
	s_addc_u32 s7, s9, s7
	v_lshlrev_b32_e32 v150, 4, v1
	v_mov_b32_e32 v151, 0
	v_lshl_add_u64 v[34:35], s[6:7], 0, v[150:151]
	s_movk_i32 s8, 0x1000
	v_add_co_u32_e32 v94, vcc, s8, v34
	s_movk_i32 s8, 0x2000
	s_nop 0
	v_addc_co_u32_e32 v95, vcc, 0, v35, vcc
	v_add_co_u32_e32 v118, vcc, s8, v34
	s_movk_i32 s8, 0x3000
	s_nop 0
	v_addc_co_u32_e32 v119, vcc, 0, v35, vcc
	v_add_co_u32_e32 v96, vcc, s8, v34
	s_movk_i32 s8, 0x4000
	s_nop 0
	v_addc_co_u32_e32 v97, vcc, 0, v35, vcc
	v_add_co_u32_e32 v98, vcc, s8, v34
	s_movk_i32 s8, 0x5000
	s_nop 0
	v_addc_co_u32_e32 v99, vcc, 0, v35, vcc
	v_add_co_u32_e32 v100, vcc, s8, v34
	s_movk_i32 s8, 0x6000
	s_nop 0
	v_addc_co_u32_e32 v101, vcc, 0, v35, vcc
	v_add_co_u32_e32 v102, vcc, s8, v34
	global_load_dwordx4 v[2:5], v[94:95], off offset:1024
	global_load_dwordx4 v[6:9], v[94:95], off offset:2048
	v_addc_co_u32_e32 v103, vcc, 0, v35, vcc
	v_add_co_u32_e32 v120, vcc, 0x7000, v34
	global_load_dwordx4 v[10:13], v[118:119], off
	global_load_dwordx4 v[14:17], v[118:119], off offset:1024
	global_load_dwordx4 v[18:21], v[96:97], off offset:3072
	global_load_dwordx4 v[22:25], v[98:99], off offset:1024
	global_load_dwordx4 v[26:29], v[118:119], off offset:2048
	global_load_dwordx4 v[30:33], v[118:119], off offset:3072
	v_addc_co_u32_e32 v121, vcc, 0, v35, vcc
	global_load_dwordx4 v[34:37], v[98:99], off offset:2048
	global_load_dwordx4 v[38:41], v[98:99], off offset:3072
	global_load_dwordx4 v[42:45], v[96:97], off offset:1024
	global_load_dwordx4 v[46:49], v[96:97], off offset:2048
	global_load_dwordx4 v[50:53], v[94:95], off offset:3072
	global_load_dwordx4 v[54:57], v[96:97], off
	global_load_dwordx4 v[58:61], v[100:101], off offset:-4096
	global_load_dwordx4 v[62:65], v[100:101], off
	global_load_dwordx4 v[66:69], v[100:101], off offset:1024
	global_load_dwordx4 v[70:73], v[100:101], off offset:2048
	global_load_dwordx4 v[74:77], v[100:101], off offset:3072
	global_load_dwordx4 v[78:81], v[102:103], off offset:2048
	global_load_dwordx4 v[82:85], v[102:103], off offset:3072
	global_load_dwordx4 v[86:89], v[102:103], off offset:1024
	global_load_dwordx4 v[90:93], v[102:103], off
	global_load_dwordx4 v[94:97], v[120:121], off
	global_load_dwordx4 v[98:101], v150, s[6:7]
	s_nop 0
	global_load_dwordx4 v[102:105], v[118:119], off offset:-4096
	global_load_dwordx4 v[106:109], v150, s[6:7] offset:3072
	global_load_dwordx4 v[110:113], v150, s[6:7] offset:1024
	global_load_dwordx4 v[114:117], v150, s[6:7] offset:2048
	s_movk_i32 s6, 0x80
	v_cmp_gt_u32_e32 vcc, s6, v0
	s_and_saveexec_b64 s[6:7], vcc
	s_cbranch_execz .LBB6_2
.LBB6_2:
	s_or_b64 exec, exec, s[6:7]
	v_cmp_gt_u32_e32 vcc, 64, v0
	v_lshl_add_u32 v118, v0, 4, 0
	s_and_saveexec_b64 s[6:7], vcc
	s_cbranch_execz .LBB6_4
	v_mov_b32_e32 v120, 0
	v_add_u32_e32 v119, 0x25400, v118
	v_mov_b32_e32 v121, v120
	v_mov_b32_e32 v122, v120
	v_mov_b32_e32 v123, v120
	ds_write_b128 v119, v[120:123]
